# hot MFMA loop headers aligned to 64B+24 (code placement)
# baseline (speedup 1.0000x reference)
.LBB0_191:
	v_mov_b32_e32 v149, v135
	v_mov_b32_e32 v147, v135
	s_add_u32 s27, s28, 0x10000
	v_mov_b32_e32 v10, 0
	s_addc_u32 s51, s29, 0
	s_mov_b32 s52, -2
	s_mov_b64 s[4:5], 0
	v_mov_b32_e32 v11, v10
	v_mov_b32_e32 v12, v10
	v_mov_b32_e32 v13, v10
	v_mov_b32_e32 v18, v10
	v_mov_b32_e32 v19, v10
	v_mov_b32_e32 v20, v10
	v_mov_b32_e32 v21, v10
	v_mov_b32_e32 v26, v10
	v_mov_b32_e32 v27, v10
	v_mov_b32_e32 v28, v10
	v_mov_b32_e32 v29, v10
	v_mov_b32_e32 v42, v10
	v_mov_b32_e32 v43, v10
	v_mov_b32_e32 v44, v10
	v_mov_b32_e32 v45, v10
	v_mov_b32_e32 v2, v10
	v_mov_b32_e32 v3, v10
	v_mov_b32_e32 v4, v10
	v_mov_b32_e32 v5, v10
	v_mov_b32_e32 v6, v10
	v_mov_b32_e32 v7, v10
	v_mov_b32_e32 v8, v10
	v_mov_b32_e32 v9, v10
	v_mov_b32_e32 v14, v10
	v_mov_b32_e32 v15, v10
	v_mov_b32_e32 v16, v10
	v_mov_b32_e32 v17, v10
	v_mov_b32_e32 v22, v10
	v_mov_b32_e32 v23, v10
	v_mov_b32_e32 v24, v10
	v_mov_b32_e32 v25, v10
	v_mov_b32_e32 v30, v10
	v_mov_b32_e32 v31, v10
	v_mov_b32_e32 v32, v10
	v_mov_b32_e32 v33, v10
	v_mov_b32_e32 v46, v10
	v_mov_b32_e32 v47, v10
	v_mov_b32_e32 v48, v10
	v_mov_b32_e32 v49, v10
	v_mov_b32_e32 v58, v10
	v_mov_b32_e32 v59, v10
	v_mov_b32_e32 v60, v10
	v_mov_b32_e32 v61, v10
	v_mov_b32_e32 v62, v10
	v_mov_b32_e32 v63, v10
	v_mov_b32_e32 v64, v10
	v_mov_b32_e32 v65, v10
	v_mov_b32_e32 v66, v10
	v_mov_b32_e32 v67, v10
	v_mov_b32_e32 v68, v10
	v_mov_b32_e32 v69, v10
	v_mov_b32_e32 v70, v10
	v_mov_b32_e32 v71, v10
	v_mov_b32_e32 v72, v10
	v_mov_b32_e32 v73, v10
	v_mov_b32_e32 v74, v10
	v_mov_b32_e32 v75, v10
	v_mov_b32_e32 v76, v10
	v_mov_b32_e32 v77, v10
	v_mov_b32_e32 v82, v10
	v_mov_b32_e32 v83, v10
	v_mov_b32_e32 v84, v10
	v_mov_b32_e32 v85, v10
	v_mov_b32_e32 v90, v10
	v_mov_b32_e32 v91, v10
	v_mov_b32_e32 v92, v10
	v_mov_b32_e32 v93, v10
	v_mov_b32_e32 v98, v10
	v_mov_b32_e32 v99, v10
	v_mov_b32_e32 v100, v10
	v_mov_b32_e32 v101, v10
	v_mov_b32_e32 v106, v10
	v_mov_b32_e32 v107, v10
	v_mov_b32_e32 v108, v10
	v_mov_b32_e32 v109, v10
	v_mov_b32_e32 v114, v10
	v_mov_b32_e32 v115, v10
	v_mov_b32_e32 v116, v10
	v_mov_b32_e32 v117, v10
	v_mov_b32_e32 v78, v10
	v_mov_b32_e32 v79, v10
	v_mov_b32_e32 v80, v10
	v_mov_b32_e32 v81, v10
	v_mov_b32_e32 v86, v10
	v_mov_b32_e32 v87, v10
	v_mov_b32_e32 v88, v10
	v_mov_b32_e32 v89, v10
	v_mov_b32_e32 v94, v10
	v_mov_b32_e32 v95, v10
	v_mov_b32_e32 v96, v10
	v_mov_b32_e32 v97, v10
	v_mov_b32_e32 v102, v10
	v_mov_b32_e32 v103, v10
	v_mov_b32_e32 v104, v10
	v_mov_b32_e32 v105, v10
	v_mov_b32_e32 v110, v10
	v_mov_b32_e32 v111, v10
	v_mov_b32_e32 v112, v10
	v_mov_b32_e32 v113, v10
	v_mov_b32_e32 v118, v10
	v_mov_b32_e32 v119, v10
	v_mov_b32_e32 v120, v10
	v_mov_b32_e32 v121, v10
	v_mov_b32_e32 v122, v10
	v_mov_b32_e32 v123, v10
	v_mov_b32_e32 v124, v10
	v_mov_b32_e32 v125, v10
	v_mov_b32_e32 v126, v10
	v_mov_b32_e32 v127, v10
	v_mov_b32_e32 v128, v10
	v_mov_b32_e32 v129, v10
	v_mov_b32_e32 v54, v10
	v_mov_b32_e32 v55, v10
	v_mov_b32_e32 v56, v10
	v_mov_b32_e32 v57, v10
	v_mov_b32_e32 v50, v10
	v_mov_b32_e32 v51, v10
	v_mov_b32_e32 v52, v10
	v_mov_b32_e32 v53, v10
	v_mov_b32_e32 v38, v10
	v_mov_b32_e32 v39, v10
	v_mov_b32_e32 v40, v10
	v_mov_b32_e32 v41, v10
	v_mov_b32_e32 v34, v10
	v_mov_b32_e32 v35, v10
	v_mov_b32_e32 v36, v10
	v_mov_b32_e32 v37, v10
	v_lshl_add_u64 v[150:151], s[14:15], 0, v[146:147]
	v_lshl_add_u64 v[152:153], s[14:15], 0, v[148:149]
	.p2align 6
	s_nop 0
	s_nop 0
	s_nop 0
	s_nop 0
	s_nop 0
	s_nop 0

.LBB0_477:
	v_mov_b32_e32 v10, 0
	v_mov_b32_e32 v133, v151
	v_mov_b32_e32 v131, v151
	s_mov_b32 s21, 0
	s_mov_b64 s[24:25], -1
	s_mov_b64 s[26:27], 0
	v_mov_b32_e32 v11, v10
	v_mov_b32_e32 v12, v10
	v_mov_b32_e32 v13, v10
	v_mov_b32_e32 v22, v10
	v_mov_b32_e32 v23, v10
	v_mov_b32_e32 v24, v10
	v_mov_b32_e32 v25, v10
	v_mov_b32_e32 v38, v10
	v_mov_b32_e32 v39, v10
	v_mov_b32_e32 v40, v10
	v_mov_b32_e32 v41, v10
	v_mov_b32_e32 v54, v10
	v_mov_b32_e32 v55, v10
	v_mov_b32_e32 v56, v10
	v_mov_b32_e32 v57, v10
	v_mov_b32_e32 v2, v10
	v_mov_b32_e32 v3, v10
	v_mov_b32_e32 v4, v10
	v_mov_b32_e32 v5, v10
	v_mov_b32_e32 v6, v10
	v_mov_b32_e32 v7, v10
	v_mov_b32_e32 v8, v10
	v_mov_b32_e32 v9, v10
	v_mov_b32_e32 v14, v10
	v_mov_b32_e32 v15, v10
	v_mov_b32_e32 v16, v10
	v_mov_b32_e32 v17, v10
	v_mov_b32_e32 v18, v10
	v_mov_b32_e32 v19, v10
	v_mov_b32_e32 v20, v10
	v_mov_b32_e32 v21, v10
	v_mov_b32_e32 v34, v10
	v_mov_b32_e32 v35, v10
	v_mov_b32_e32 v36, v10
	v_mov_b32_e32 v37, v10
	v_mov_b32_e32 v42, v10
	v_mov_b32_e32 v43, v10
	v_mov_b32_e32 v44, v10
	v_mov_b32_e32 v45, v10
	v_mov_b32_e32 v58, v10
	v_mov_b32_e32 v59, v10
	v_mov_b32_e32 v60, v10
	v_mov_b32_e32 v61, v10
	v_mov_b32_e32 v62, v10
	v_mov_b32_e32 v63, v10
	v_mov_b32_e32 v64, v10
	v_mov_b32_e32 v65, v10
	v_mov_b32_e32 v66, v10
	v_mov_b32_e32 v67, v10
	v_mov_b32_e32 v68, v10
	v_mov_b32_e32 v69, v10
	v_mov_b32_e32 v70, v10
	v_mov_b32_e32 v71, v10
	v_mov_b32_e32 v72, v10
	v_mov_b32_e32 v73, v10
	v_mov_b32_e32 v74, v10
	v_mov_b32_e32 v75, v10
	v_mov_b32_e32 v76, v10
	v_mov_b32_e32 v77, v10
	v_mov_b32_e32 v78, v10
	v_mov_b32_e32 v79, v10
	v_mov_b32_e32 v80, v10
	v_mov_b32_e32 v81, v10
	v_mov_b32_e32 v82, v10
	v_mov_b32_e32 v83, v10
	v_mov_b32_e32 v84, v10
	v_mov_b32_e32 v85, v10
	v_mov_b32_e32 v90, v10
	v_mov_b32_e32 v91, v10
	v_mov_b32_e32 v92, v10
	v_mov_b32_e32 v93, v10
	v_mov_b32_e32 v98, v10
	v_mov_b32_e32 v99, v10
	v_mov_b32_e32 v100, v10
	v_mov_b32_e32 v101, v10
	v_mov_b32_e32 v106, v10
	v_mov_b32_e32 v107, v10
	v_mov_b32_e32 v108, v10
	v_mov_b32_e32 v109, v10
	v_mov_b32_e32 v86, v10
	v_mov_b32_e32 v87, v10
	v_mov_b32_e32 v88, v10
	v_mov_b32_e32 v89, v10
	v_mov_b32_e32 v94, v10
	v_mov_b32_e32 v95, v10
	v_mov_b32_e32 v96, v10
	v_mov_b32_e32 v97, v10
	v_mov_b32_e32 v102, v10
	v_mov_b32_e32 v103, v10
	v_mov_b32_e32 v104, v10
	v_mov_b32_e32 v105, v10
	v_mov_b32_e32 v110, v10
	v_mov_b32_e32 v111, v10
	v_mov_b32_e32 v112, v10
	v_mov_b32_e32 v113, v10
	v_mov_b32_e32 v114, v10
	v_mov_b32_e32 v115, v10
	v_mov_b32_e32 v116, v10
	v_mov_b32_e32 v117, v10
	v_mov_b32_e32 v118, v10
	v_mov_b32_e32 v119, v10
	v_mov_b32_e32 v120, v10
	v_mov_b32_e32 v121, v10
	v_mov_b32_e32 v122, v10
	v_mov_b32_e32 v123, v10
	v_mov_b32_e32 v124, v10
	v_mov_b32_e32 v125, v10
	v_mov_b32_e32 v126, v10
	v_mov_b32_e32 v127, v10
	v_mov_b32_e32 v128, v10
	v_mov_b32_e32 v129, v10
	v_mov_b32_e32 v46, v10
	v_mov_b32_e32 v47, v10
	v_mov_b32_e32 v48, v10
	v_mov_b32_e32 v49, v10
	v_mov_b32_e32 v50, v10
	v_mov_b32_e32 v51, v10
	v_mov_b32_e32 v52, v10
	v_mov_b32_e32 v53, v10
	v_mov_b32_e32 v26, v10
	v_mov_b32_e32 v27, v10
	v_mov_b32_e32 v28, v10
	v_mov_b32_e32 v29, v10
	v_mov_b32_e32 v30, v10
	v_mov_b32_e32 v31, v10
	v_mov_b32_e32 v32, v10
	v_mov_b32_e32 v33, v10
	.p2align 6
	s_nop 0
	s_nop 0
	s_nop 0
	s_nop 0
	s_nop 0
	s_nop 0

.LBB0_619:
	v_mov_b32_e32 v143, v135
	v_mov_b32_e32 v141, v135
	s_add_u32 s7, s34, 0x10000
	v_mov_b32_e32 v10, 0
	s_addc_u32 s27, s35, 0
	v_lshl_add_u64 v[144:145], s[14:15], 0, v[140:141]
	v_lshl_add_u64 v[146:147], s[14:15], 0, v[142:143]
	s_mov_b32 s29, -2
	s_mov_b64 s[34:35], 0
	v_mov_b32_e32 v11, v10
	v_mov_b32_e32 v12, v10
	v_mov_b32_e32 v13, v10
	v_mov_b32_e32 v18, v10
	v_mov_b32_e32 v19, v10
	v_mov_b32_e32 v20, v10
	v_mov_b32_e32 v21, v10
	v_mov_b32_e32 v30, v10
	v_mov_b32_e32 v31, v10
	v_mov_b32_e32 v32, v10
	v_mov_b32_e32 v33, v10
	v_mov_b32_e32 v42, v10
	v_mov_b32_e32 v43, v10
	v_mov_b32_e32 v44, v10
	v_mov_b32_e32 v45, v10
	v_mov_b32_e32 v2, v10
	v_mov_b32_e32 v3, v10
	v_mov_b32_e32 v4, v10
	v_mov_b32_e32 v5, v10
	v_mov_b32_e32 v6, v10
	v_mov_b32_e32 v7, v10
	v_mov_b32_e32 v8, v10
	v_mov_b32_e32 v9, v10
	v_mov_b32_e32 v14, v10
	v_mov_b32_e32 v15, v10
	v_mov_b32_e32 v16, v10
	v_mov_b32_e32 v17, v10
	v_mov_b32_e32 v22, v10
	v_mov_b32_e32 v23, v10
	v_mov_b32_e32 v24, v10
	v_mov_b32_e32 v25, v10
	v_mov_b32_e32 v38, v10
	v_mov_b32_e32 v39, v10
	v_mov_b32_e32 v40, v10
	v_mov_b32_e32 v41, v10
	v_mov_b32_e32 v46, v10
	v_mov_b32_e32 v47, v10
	v_mov_b32_e32 v48, v10
	v_mov_b32_e32 v49, v10
	v_mov_b32_e32 v58, v10
	v_mov_b32_e32 v59, v10
	v_mov_b32_e32 v60, v10
	v_mov_b32_e32 v61, v10
	v_mov_b32_e32 v62, v10
	v_mov_b32_e32 v63, v10
	v_mov_b32_e32 v64, v10
	v_mov_b32_e32 v65, v10
	v_mov_b32_e32 v66, v10
	v_mov_b32_e32 v67, v10
	v_mov_b32_e32 v68, v10
	v_mov_b32_e32 v69, v10
	v_mov_b32_e32 v70, v10
	v_mov_b32_e32 v71, v10
	v_mov_b32_e32 v72, v10
	v_mov_b32_e32 v73, v10
	v_mov_b32_e32 v74, v10
	v_mov_b32_e32 v75, v10
	v_mov_b32_e32 v76, v10
	v_mov_b32_e32 v77, v10
	v_mov_b32_e32 v82, v10
	v_mov_b32_e32 v83, v10
	v_mov_b32_e32 v84, v10
	v_mov_b32_e32 v85, v10
	v_mov_b32_e32 v90, v10
	v_mov_b32_e32 v91, v10
	v_mov_b32_e32 v92, v10
	v_mov_b32_e32 v93, v10
	v_mov_b32_e32 v98, v10
	v_mov_b32_e32 v99, v10
	v_mov_b32_e32 v100, v10
	v_mov_b32_e32 v101, v10
	v_mov_b32_e32 v106, v10
	v_mov_b32_e32 v107, v10
	v_mov_b32_e32 v108, v10
	v_mov_b32_e32 v109, v10
	v_mov_b32_e32 v114, v10
	v_mov_b32_e32 v115, v10
	v_mov_b32_e32 v116, v10
	v_mov_b32_e32 v117, v10
	v_mov_b32_e32 v78, v10
	v_mov_b32_e32 v79, v10
	v_mov_b32_e32 v80, v10
	v_mov_b32_e32 v81, v10
	v_mov_b32_e32 v86, v10
	v_mov_b32_e32 v87, v10
	v_mov_b32_e32 v88, v10
	v_mov_b32_e32 v89, v10
	v_mov_b32_e32 v94, v10
	v_mov_b32_e32 v95, v10
	v_mov_b32_e32 v96, v10
	v_mov_b32_e32 v97, v10
	v_mov_b32_e32 v102, v10
	v_mov_b32_e32 v103, v10
	v_mov_b32_e32 v104, v10
	v_mov_b32_e32 v105, v10
	v_mov_b32_e32 v110, v10
	v_mov_b32_e32 v111, v10
	v_mov_b32_e32 v112, v10
	v_mov_b32_e32 v113, v10
	v_mov_b32_e32 v118, v10
	v_mov_b32_e32 v119, v10
	v_mov_b32_e32 v120, v10
	v_mov_b32_e32 v121, v10
	v_mov_b32_e32 v122, v10
	v_mov_b32_e32 v123, v10
	v_mov_b32_e32 v124, v10
	v_mov_b32_e32 v125, v10
	v_mov_b32_e32 v126, v10
	v_mov_b32_e32 v127, v10
	v_mov_b32_e32 v128, v10
	v_mov_b32_e32 v129, v10
	v_mov_b32_e32 v54, v10
	v_mov_b32_e32 v55, v10
	v_mov_b32_e32 v56, v10
	v_mov_b32_e32 v57, v10
	v_mov_b32_e32 v50, v10
	v_mov_b32_e32 v51, v10
	v_mov_b32_e32 v52, v10
	v_mov_b32_e32 v53, v10
	v_mov_b32_e32 v34, v10
	v_mov_b32_e32 v35, v10
	v_mov_b32_e32 v36, v10
	v_mov_b32_e32 v37, v10
	v_mov_b32_e32 v26, v10
	v_mov_b32_e32 v27, v10
	v_mov_b32_e32 v28, v10
	v_mov_b32_e32 v29, v10
	.p2align 6
	s_nop 0
	s_nop 0
	s_nop 0
	s_nop 0
	s_nop 0
	s_nop 0

.LBB0_925:
	v_mov_b32_e32 v4, v3
	v_mov_b32_e32 v5, v3
	v_mov_b32_e32 v215, v3
	v_mov_b32_e32 v213, v3
	s_add_u32 s25, s6, 0x10000
	v_mov_b32_e32 v2, v3
	v_mov_b32_e32 v70, 0
	v_cmp_eq_u32_e64 s[4:5], 0, v6
	v_mov_b64_e32 v[40:41], v[4:5]
	v_mov_b64_e32 v[48:49], v[4:5]
	v_mov_b64_e32 v[56:57], v[4:5]
	v_mov_b64_e32 v[64:65], v[4:5]
	v_mov_b64_e32 v[8:9], v[4:5]
	v_mov_b64_e32 v[16:17], v[4:5]
	v_mov_b64_e32 v[24:25], v[4:5]
	v_mov_b64_e32 v[32:33], v[4:5]
	v_mov_b64_e32 v[44:45], v[4:5]
	v_mov_b64_e32 v[52:53], v[4:5]
	v_mov_b64_e32 v[60:61], v[4:5]
	v_mov_b64_e32 v[68:69], v[4:5]
	v_mov_b64_e32 v[36:37], v[4:5]
	v_mov_b64_e32 v[28:29], v[4:5]
	v_mov_b64_e32 v[20:21], v[4:5]
	v_mov_b64_e32 v[12:13], v[4:5]
	s_addc_u32 s27, s7, 0
	v_lshl_add_u64 v[218:219], s[18:19], 0, v[212:213]
	v_lshl_add_u64 v[220:221], s[18:19], 0, v[214:215]
	s_mov_b32 s58, -2
	s_mov_b64 s[28:29], 0
	v_cndmask_b32_e64 v213, 0, 1, s[4:5]
	v_mov_b64_e32 v[38:39], v[2:3]
	v_mov_b64_e32 v[46:47], v[2:3]
	v_mov_b64_e32 v[54:55], v[2:3]
	v_mov_b64_e32 v[62:63], v[2:3]
	v_mov_b64_e32 v[6:7], v[2:3]
	v_mov_b64_e32 v[14:15], v[2:3]
	v_mov_b64_e32 v[22:23], v[2:3]
	v_mov_b64_e32 v[30:31], v[2:3]
	v_mov_b64_e32 v[42:43], v[2:3]
	v_mov_b64_e32 v[50:51], v[2:3]
	v_mov_b64_e32 v[58:59], v[2:3]
	v_mov_b64_e32 v[66:67], v[2:3]
	v_mov_b64_e32 v[34:35], v[2:3]
	v_mov_b64_e32 v[26:27], v[2:3]
	v_mov_b64_e32 v[18:19], v[2:3]
	v_mov_b64_e32 v[10:11], v[2:3]
	v_mov_b32_e32 v71, v70
	v_mov_b32_e32 v72, v70
	v_mov_b32_e32 v73, v70
	v_mov_b32_e32 v78, v70
	v_mov_b32_e32 v79, v70
	v_mov_b32_e32 v80, v70
	v_mov_b32_e32 v81, v70
	v_mov_b32_e32 v86, v70
	v_mov_b32_e32 v87, v70
	v_mov_b32_e32 v88, v70
	v_mov_b32_e32 v89, v70
	v_mov_b32_e32 v94, v70
	v_mov_b32_e32 v95, v70
	v_mov_b32_e32 v96, v70
	v_mov_b32_e32 v97, v70
	v_mov_b32_e32 v102, v70
	v_mov_b32_e32 v103, v70
	v_mov_b32_e32 v104, v70
	v_mov_b32_e32 v105, v70
	v_mov_b32_e32 v110, v70
	v_mov_b32_e32 v111, v70
	v_mov_b32_e32 v112, v70
	v_mov_b32_e32 v113, v70
	v_mov_b32_e32 v118, v70
	v_mov_b32_e32 v119, v70
	v_mov_b32_e32 v120, v70
	v_mov_b32_e32 v121, v70
	v_mov_b32_e32 v126, v70
	v_mov_b32_e32 v127, v70
	v_mov_b32_e32 v128, v70
	v_mov_b32_e32 v129, v70
	v_mov_b32_e32 v74, v70
	v_mov_b32_e32 v75, v70
	v_mov_b32_e32 v76, v70
	v_mov_b32_e32 v77, v70
	v_mov_b32_e32 v82, v70
	v_mov_b32_e32 v83, v70
	v_mov_b32_e32 v84, v70
	v_mov_b32_e32 v85, v70
	v_mov_b32_e32 v90, v70
	v_mov_b32_e32 v91, v70
	v_mov_b32_e32 v92, v70
	v_mov_b32_e32 v93, v70
	v_mov_b32_e32 v98, v70
	v_mov_b32_e32 v99, v70
	v_mov_b32_e32 v100, v70
	v_mov_b32_e32 v101, v70
	v_mov_b32_e32 v106, v70
	v_mov_b32_e32 v107, v70
	v_mov_b32_e32 v108, v70
	v_mov_b32_e32 v109, v70
	v_mov_b32_e32 v114, v70
	v_mov_b32_e32 v115, v70
	v_mov_b32_e32 v116, v70
	v_mov_b32_e32 v117, v70
	v_mov_b32_e32 v122, v70
	v_mov_b32_e32 v123, v70
	v_mov_b32_e32 v124, v70
	v_mov_b32_e32 v125, v70
	v_mov_b32_e32 v130, v70
	v_mov_b32_e32 v131, v70
	v_mov_b32_e32 v132, v70
	v_mov_b32_e32 v133, v70
	s_branch .LBB0_927
	.p2align 6
	s_nop 0
	s_nop 0
	s_nop 0
	s_nop 0
	s_nop 0
	s_nop 0

.LBB0_1002:
	v_mov_b32_e32 v4, v3
	v_mov_b32_e32 v5, v3
	v_mov_b32_e32 v2, v3
	v_mov_b64_e32 v[38:39], v[4:5]
	v_mov_b64_e32 v[42:43], v[4:5]
	v_mov_b64_e32 v[54:55], v[4:5]
	v_mov_b64_e32 v[58:59], v[4:5]
	v_mov_b64_e32 v[14:15], v[4:5]
	v_mov_b64_e32 v[18:19], v[4:5]
	v_mov_b64_e32 v[30:31], v[4:5]
	v_mov_b64_e32 v[34:35], v[4:5]
	v_mov_b64_e32 v[46:47], v[4:5]
	v_mov_b64_e32 v[50:51], v[4:5]
	v_mov_b64_e32 v[62:63], v[4:5]
	v_mov_b64_e32 v[66:67], v[4:5]
	v_mov_b64_e32 v[26:27], v[4:5]
	v_mov_b64_e32 v[22:23], v[4:5]
	v_mov_b64_e32 v[10:11], v[4:5]
	v_mov_b32_e32 v211, v3
	v_mov_b32_e32 v209, v3
	s_add_u32 s31, s6, 0x10000
	v_mov_b32_e32 v68, 0
	v_cmp_eq_u32_e64 s[4:5], 0, v6
	v_mov_b64_e32 v[36:37], v[2:3]
	v_mov_b64_e32 v[40:41], v[2:3]
	v_mov_b64_e32 v[52:53], v[2:3]
	v_mov_b64_e32 v[56:57], v[2:3]
	v_mov_b64_e32 v[12:13], v[2:3]
	v_mov_b64_e32 v[16:17], v[2:3]
	v_mov_b64_e32 v[28:29], v[2:3]
	v_mov_b64_e32 v[32:33], v[2:3]
	v_mov_b64_e32 v[44:45], v[2:3]
	v_mov_b64_e32 v[48:49], v[2:3]
	v_mov_b64_e32 v[60:61], v[2:3]
	v_mov_b64_e32 v[64:65], v[2:3]
	v_mov_b64_e32 v[24:25], v[2:3]
	v_mov_b64_e32 v[20:21], v[2:3]
	v_mov_b64_e32 v[8:9], v[2:3]
	v_mov_b64_e32 v[6:7], v[4:5]
	s_addc_u32 s35, s7, 0
	v_lshl_add_u64 v[212:213], s[16:17], 0, v[208:209]
	v_lshl_add_u64 v[214:215], s[16:17], 0, v[210:211]
	s_mov_b32 s65, -2
	s_mov_b64 s[38:39], 0
	v_cndmask_b32_e64 v209, 0, 1, s[4:5]
	v_mov_b64_e32 v[4:5], v[2:3]
	v_mov_b32_e32 v69, v68
	v_mov_b32_e32 v70, v68
	v_mov_b32_e32 v71, v68
	v_mov_b32_e32 v72, v68
	v_mov_b32_e32 v73, v68
	v_mov_b32_e32 v74, v68
	v_mov_b32_e32 v75, v68
	v_mov_b32_e32 v76, v68
	v_mov_b32_e32 v77, v68
	v_mov_b32_e32 v78, v68
	v_mov_b32_e32 v79, v68
	v_mov_b32_e32 v84, v68
	v_mov_b32_e32 v85, v68
	v_mov_b32_e32 v86, v68
	v_mov_b32_e32 v87, v68
	v_mov_b32_e32 v92, v68
	v_mov_b32_e32 v93, v68
	v_mov_b32_e32 v94, v68
	v_mov_b32_e32 v95, v68
	v_mov_b32_e32 v100, v68
	v_mov_b32_e32 v101, v68
	v_mov_b32_e32 v102, v68
	v_mov_b32_e32 v103, v68
	v_mov_b32_e32 v108, v68
	v_mov_b32_e32 v109, v68
	v_mov_b32_e32 v110, v68
	v_mov_b32_e32 v111, v68
	v_mov_b32_e32 v116, v68
	v_mov_b32_e32 v117, v68
	v_mov_b32_e32 v118, v68
	v_mov_b32_e32 v119, v68
	v_mov_b32_e32 v80, v68
	v_mov_b32_e32 v81, v68
	v_mov_b32_e32 v82, v68
	v_mov_b32_e32 v83, v68
	v_mov_b32_e32 v88, v68
	v_mov_b32_e32 v89, v68
	v_mov_b32_e32 v90, v68
	v_mov_b32_e32 v91, v68
	v_mov_b32_e32 v96, v68
	v_mov_b32_e32 v97, v68
	v_mov_b32_e32 v98, v68
	v_mov_b32_e32 v99, v68
	v_mov_b32_e32 v104, v68
	v_mov_b32_e32 v105, v68
	v_mov_b32_e32 v106, v68
	v_mov_b32_e32 v107, v68
	v_mov_b32_e32 v112, v68
	v_mov_b32_e32 v113, v68
	v_mov_b32_e32 v114, v68
	v_mov_b32_e32 v115, v68
	v_mov_b32_e32 v120, v68
	v_mov_b32_e32 v121, v68
	v_mov_b32_e32 v122, v68
	v_mov_b32_e32 v123, v68
	v_mov_b32_e32 v124, v68
	v_mov_b32_e32 v125, v68
	v_mov_b32_e32 v126, v68
	v_mov_b32_e32 v127, v68
	v_mov_b32_e32 v128, v68
	v_mov_b32_e32 v129, v68
	v_mov_b32_e32 v130, v68
	v_mov_b32_e32 v131, v68
	s_branch .LBB0_1004
	.p2align 6
	s_nop 0
	s_nop 0
	s_nop 0
	s_nop 0
	s_nop 0
	s_nop 0

.LBB0_1149:
	v_mov_b32_e32 v147, v135
	v_mov_b32_e32 v145, v135
	s_add_u32 s19, s22, 0x10000
	v_mov_b32_e32 v10, 0
	s_addc_u32 s46, s23, 0
	v_lshl_add_u64 v[148:149], s[12:13], 0, v[144:145]
	v_lshl_add_u64 v[150:151], s[12:13], 0, v[146:147]
	s_mov_b32 s47, -2
	s_mov_b64 s[22:23], 0
	v_mov_b32_e32 v11, v10
	v_mov_b32_e32 v12, v10
	v_mov_b32_e32 v13, v10
	v_mov_b32_e32 v18, v10
	v_mov_b32_e32 v19, v10
	v_mov_b32_e32 v20, v10
	v_mov_b32_e32 v21, v10
	v_mov_b32_e32 v26, v10
	v_mov_b32_e32 v27, v10
	v_mov_b32_e32 v28, v10
	v_mov_b32_e32 v29, v10
	v_mov_b32_e32 v42, v10
	v_mov_b32_e32 v43, v10
	v_mov_b32_e32 v44, v10
	v_mov_b32_e32 v45, v10
	v_mov_b32_e32 v2, v10
	v_mov_b32_e32 v3, v10
	v_mov_b32_e32 v4, v10
	v_mov_b32_e32 v5, v10
	v_mov_b32_e32 v6, v10
	v_mov_b32_e32 v7, v10
	v_mov_b32_e32 v8, v10
	v_mov_b32_e32 v9, v10
	v_mov_b32_e32 v14, v10
	v_mov_b32_e32 v15, v10
	v_mov_b32_e32 v16, v10
	v_mov_b32_e32 v17, v10
	v_mov_b32_e32 v22, v10
	v_mov_b32_e32 v23, v10
	v_mov_b32_e32 v24, v10
	v_mov_b32_e32 v25, v10
	v_mov_b32_e32 v30, v10
	v_mov_b32_e32 v31, v10
	v_mov_b32_e32 v32, v10
	v_mov_b32_e32 v33, v10
	v_mov_b32_e32 v46, v10
	v_mov_b32_e32 v47, v10
	v_mov_b32_e32 v48, v10
	v_mov_b32_e32 v49, v10
	v_mov_b32_e32 v58, v10
	v_mov_b32_e32 v59, v10
	v_mov_b32_e32 v60, v10
	v_mov_b32_e32 v61, v10
	v_mov_b32_e32 v62, v10
	v_mov_b32_e32 v63, v10
	v_mov_b32_e32 v64, v10
	v_mov_b32_e32 v65, v10
	v_mov_b32_e32 v66, v10
	v_mov_b32_e32 v67, v10
	v_mov_b32_e32 v68, v10
	v_mov_b32_e32 v69, v10
	v_mov_b32_e32 v70, v10
	v_mov_b32_e32 v71, v10
	v_mov_b32_e32 v72, v10
	v_mov_b32_e32 v73, v10
	v_mov_b32_e32 v74, v10
	v_mov_b32_e32 v75, v10
	v_mov_b32_e32 v76, v10
	v_mov_b32_e32 v77, v10
	v_mov_b32_e32 v82, v10
	v_mov_b32_e32 v83, v10
	v_mov_b32_e32 v84, v10
	v_mov_b32_e32 v85, v10
	v_mov_b32_e32 v90, v10
	v_mov_b32_e32 v91, v10
	v_mov_b32_e32 v92, v10
	v_mov_b32_e32 v93, v10
	v_mov_b32_e32 v98, v10
	v_mov_b32_e32 v99, v10
	v_mov_b32_e32 v100, v10
	v_mov_b32_e32 v101, v10
	v_mov_b32_e32 v106, v10
	v_mov_b32_e32 v107, v10
	v_mov_b32_e32 v108, v10
	v_mov_b32_e32 v109, v10
	v_mov_b32_e32 v114, v10
	v_mov_b32_e32 v115, v10
	v_mov_b32_e32 v116, v10
	v_mov_b32_e32 v117, v10
	v_mov_b32_e32 v78, v10
	v_mov_b32_e32 v79, v10
	v_mov_b32_e32 v80, v10
	v_mov_b32_e32 v81, v10
	v_mov_b32_e32 v86, v10
	v_mov_b32_e32 v87, v10
	v_mov_b32_e32 v88, v10
	v_mov_b32_e32 v89, v10
	v_mov_b32_e32 v94, v10
	v_mov_b32_e32 v95, v10
	v_mov_b32_e32 v96, v10
	v_mov_b32_e32 v97, v10
	v_mov_b32_e32 v102, v10
	v_mov_b32_e32 v103, v10
	v_mov_b32_e32 v104, v10
	v_mov_b32_e32 v105, v10
	v_mov_b32_e32 v110, v10
	v_mov_b32_e32 v111, v10
	v_mov_b32_e32 v112, v10
	v_mov_b32_e32 v113, v10
	v_mov_b32_e32 v118, v10
	v_mov_b32_e32 v119, v10
	v_mov_b32_e32 v120, v10
	v_mov_b32_e32 v121, v10
	v_mov_b32_e32 v122, v10
	v_mov_b32_e32 v123, v10
	v_mov_b32_e32 v124, v10
	v_mov_b32_e32 v125, v10
	v_mov_b32_e32 v126, v10
	v_mov_b32_e32 v127, v10
	v_mov_b32_e32 v128, v10
	v_mov_b32_e32 v129, v10
	v_mov_b32_e32 v54, v10
	v_mov_b32_e32 v55, v10
	v_mov_b32_e32 v56, v10
	v_mov_b32_e32 v57, v10
	v_mov_b32_e32 v50, v10
	v_mov_b32_e32 v51, v10
	v_mov_b32_e32 v52, v10
	v_mov_b32_e32 v53, v10
	v_mov_b32_e32 v38, v10
	v_mov_b32_e32 v39, v10
	v_mov_b32_e32 v40, v10
	v_mov_b32_e32 v41, v10
	v_mov_b32_e32 v34, v10
	v_mov_b32_e32 v35, v10
	v_mov_b32_e32 v36, v10
	v_mov_b32_e32 v37, v10
	.p2align 6
	s_nop 0
	s_nop 0
	s_nop 0
	s_nop 0
	s_nop 0
	s_nop 0

.LBB0_1294:
	v_mov_b32_e32 v161, v139
	v_mov_b32_e32 v163, v139
	s_add_u32 s56, s0, 0x10000
	v_mov_b32_e32 v18, 0
	s_addc_u32 s57, s1, 0
	v_lshl_add_u64 v[164:165], s[22:23], 0, v[162:163]
	v_lshl_add_u64 v[166:167], s[22:23], 0, v[160:161]
	s_mov_b32 s58, -2
	s_mov_b64 s[0:1], 0
	v_mov_b32_e32 v19, v18
	v_mov_b32_e32 v20, v18
	v_mov_b32_e32 v21, v18
	v_mov_b32_e32 v22, v18
	v_mov_b32_e32 v23, v18
	v_mov_b32_e32 v24, v18
	v_mov_b32_e32 v25, v18
	v_mov_b32_e32 v26, v18
	v_mov_b32_e32 v27, v18
	v_mov_b32_e32 v28, v18
	v_mov_b32_e32 v29, v18
	v_mov_b32_e32 v30, v18
	v_mov_b32_e32 v31, v18
	v_mov_b32_e32 v32, v18
	v_mov_b32_e32 v33, v18
	v_mov_b32_e32 v66, v18
	v_mov_b32_e32 v67, v18
	v_mov_b32_e32 v68, v18
	v_mov_b32_e32 v69, v18
	v_mov_b32_e32 v70, v18
	v_mov_b32_e32 v71, v18
	v_mov_b32_e32 v72, v18
	v_mov_b32_e32 v73, v18
	v_mov_b32_e32 v74, v18
	v_mov_b32_e32 v75, v18
	v_mov_b32_e32 v76, v18
	v_mov_b32_e32 v77, v18
	v_mov_b32_e32 v78, v18
	v_mov_b32_e32 v79, v18
	v_mov_b32_e32 v80, v18
	v_mov_b32_e32 v81, v18
	v_mov_b32_e32 v82, v18
	v_mov_b32_e32 v83, v18
	v_mov_b32_e32 v84, v18
	v_mov_b32_e32 v85, v18
	v_mov_b32_e32 v86, v18
	v_mov_b32_e32 v87, v18
	v_mov_b32_e32 v88, v18
	v_mov_b32_e32 v89, v18
	v_mov_b32_e32 v90, v18
	v_mov_b32_e32 v91, v18
	v_mov_b32_e32 v92, v18
	v_mov_b32_e32 v93, v18
	v_mov_b32_e32 v94, v18
	v_mov_b32_e32 v95, v18
	v_mov_b32_e32 v96, v18
	v_mov_b32_e32 v97, v18
	v_mov_b32_e32 v34, v18
	v_mov_b32_e32 v35, v18
	v_mov_b32_e32 v36, v18
	v_mov_b32_e32 v37, v18
	v_mov_b32_e32 v38, v18
	v_mov_b32_e32 v39, v18
	v_mov_b32_e32 v40, v18
	v_mov_b32_e32 v41, v18
	v_mov_b32_e32 v42, v18
	v_mov_b32_e32 v43, v18
	v_mov_b32_e32 v44, v18
	v_mov_b32_e32 v45, v18
	v_mov_b32_e32 v46, v18
	v_mov_b32_e32 v47, v18
	v_mov_b32_e32 v48, v18
	v_mov_b32_e32 v49, v18
	v_mov_b32_e32 v50, v18
	v_mov_b32_e32 v51, v18
	v_mov_b32_e32 v52, v18
	v_mov_b32_e32 v53, v18
	v_mov_b32_e32 v54, v18
	v_mov_b32_e32 v55, v18
	v_mov_b32_e32 v56, v18
	v_mov_b32_e32 v57, v18
	v_mov_b32_e32 v58, v18
	v_mov_b32_e32 v59, v18
	v_mov_b32_e32 v60, v18
	v_mov_b32_e32 v61, v18
	v_mov_b32_e32 v62, v18
	v_mov_b32_e32 v63, v18
	v_mov_b32_e32 v64, v18
	v_mov_b32_e32 v65, v18
	v_mov_b32_e32 v98, v18
	v_mov_b32_e32 v99, v18
	v_mov_b32_e32 v100, v18
	v_mov_b32_e32 v101, v18
	v_mov_b32_e32 v102, v18
	v_mov_b32_e32 v103, v18
	v_mov_b32_e32 v104, v18
	v_mov_b32_e32 v105, v18
	v_mov_b32_e32 v106, v18
	v_mov_b32_e32 v107, v18
	v_mov_b32_e32 v108, v18
	v_mov_b32_e32 v109, v18
	v_mov_b32_e32 v110, v18
	v_mov_b32_e32 v111, v18
	v_mov_b32_e32 v112, v18
	v_mov_b32_e32 v113, v18
	v_mov_b32_e32 v114, v18
	v_mov_b32_e32 v115, v18
	v_mov_b32_e32 v116, v18
	v_mov_b32_e32 v117, v18
	v_mov_b32_e32 v118, v18
	v_mov_b32_e32 v119, v18
	v_mov_b32_e32 v120, v18
	v_mov_b32_e32 v121, v18
	v_mov_b32_e32 v122, v18
	v_mov_b32_e32 v123, v18
	v_mov_b32_e32 v124, v18
	v_mov_b32_e32 v125, v18
	v_mov_b32_e32 v126, v18
	v_mov_b32_e32 v127, v18
	v_mov_b32_e32 v128, v18
	v_mov_b32_e32 v129, v18
	v_mov_b32_e32 v10, v18
	v_mov_b32_e32 v11, v18
	v_mov_b32_e32 v12, v18
	v_mov_b32_e32 v13, v18
	v_mov_b32_e32 v14, v18
	v_mov_b32_e32 v15, v18
	v_mov_b32_e32 v16, v18
	v_mov_b32_e32 v17, v18
	v_mov_b32_e32 v2, v18
	v_mov_b32_e32 v3, v18
	v_mov_b32_e32 v4, v18
	v_mov_b32_e32 v5, v18
	v_mov_b32_e32 v6, v18
	v_mov_b32_e32 v7, v18
	v_mov_b32_e32 v8, v18
	v_mov_b32_e32 v9, v18
	.p2align 6
	s_nop 0
	s_nop 0
	s_nop 0
	s_nop 0
	s_nop 0
	s_nop 0

.LBB0_1344:
	v_mov_b32_e32 v143, v135
	v_mov_b32_e32 v145, v135
	s_add_u32 s27, s28, 0x10000
	v_mov_b32_e32 v10, 0
	s_addc_u32 s57, s29, 0
	v_lshl_add_u64 v[146:147], s[12:13], 0, v[142:143]
	v_lshl_add_u64 v[148:149], s[12:13], 0, v[144:145]
	s_mov_b32 s58, -2
	s_mov_b64 s[28:29], 0
	v_mov_b32_e32 v11, v10
	v_mov_b32_e32 v12, v10
	v_mov_b32_e32 v13, v10
	v_mov_b32_e32 v18, v10
	v_mov_b32_e32 v19, v10
	v_mov_b32_e32 v20, v10
	v_mov_b32_e32 v21, v10
	v_mov_b32_e32 v30, v10
	v_mov_b32_e32 v31, v10
	v_mov_b32_e32 v32, v10
	v_mov_b32_e32 v33, v10
	v_mov_b32_e32 v42, v10
	v_mov_b32_e32 v43, v10
	v_mov_b32_e32 v44, v10
	v_mov_b32_e32 v45, v10
	v_mov_b32_e32 v2, v10
	v_mov_b32_e32 v3, v10
	v_mov_b32_e32 v4, v10
	v_mov_b32_e32 v5, v10
	v_mov_b32_e32 v6, v10
	v_mov_b32_e32 v7, v10
	v_mov_b32_e32 v8, v10
	v_mov_b32_e32 v9, v10
	v_mov_b32_e32 v14, v10
	v_mov_b32_e32 v15, v10
	v_mov_b32_e32 v16, v10
	v_mov_b32_e32 v17, v10
	v_mov_b32_e32 v22, v10
	v_mov_b32_e32 v23, v10
	v_mov_b32_e32 v24, v10
	v_mov_b32_e32 v25, v10
	v_mov_b32_e32 v38, v10
	v_mov_b32_e32 v39, v10
	v_mov_b32_e32 v40, v10
	v_mov_b32_e32 v41, v10
	v_mov_b32_e32 v46, v10
	v_mov_b32_e32 v47, v10
	v_mov_b32_e32 v48, v10
	v_mov_b32_e32 v49, v10
	v_mov_b32_e32 v58, v10
	v_mov_b32_e32 v59, v10
	v_mov_b32_e32 v60, v10
	v_mov_b32_e32 v61, v10
	v_mov_b32_e32 v62, v10
	v_mov_b32_e32 v63, v10
	v_mov_b32_e32 v64, v10
	v_mov_b32_e32 v65, v10
	v_mov_b32_e32 v66, v10
	v_mov_b32_e32 v67, v10
	v_mov_b32_e32 v68, v10
	v_mov_b32_e32 v69, v10
	v_mov_b32_e32 v70, v10
	v_mov_b32_e32 v71, v10
	v_mov_b32_e32 v72, v10
	v_mov_b32_e32 v73, v10
	v_mov_b32_e32 v74, v10
	v_mov_b32_e32 v75, v10
	v_mov_b32_e32 v76, v10
	v_mov_b32_e32 v77, v10
	v_mov_b32_e32 v82, v10
	v_mov_b32_e32 v83, v10
	v_mov_b32_e32 v84, v10
	v_mov_b32_e32 v85, v10
	v_mov_b32_e32 v90, v10
	v_mov_b32_e32 v91, v10
	v_mov_b32_e32 v92, v10
	v_mov_b32_e32 v93, v10
	v_mov_b32_e32 v98, v10
	v_mov_b32_e32 v99, v10
	v_mov_b32_e32 v100, v10
	v_mov_b32_e32 v101, v10
	v_mov_b32_e32 v106, v10
	v_mov_b32_e32 v107, v10
	v_mov_b32_e32 v108, v10
	v_mov_b32_e32 v109, v10
	v_mov_b32_e32 v114, v10
	v_mov_b32_e32 v115, v10
	v_mov_b32_e32 v116, v10
	v_mov_b32_e32 v117, v10
	v_mov_b32_e32 v78, v10
	v_mov_b32_e32 v79, v10
	v_mov_b32_e32 v80, v10
	v_mov_b32_e32 v81, v10
	v_mov_b32_e32 v86, v10
	v_mov_b32_e32 v87, v10
	v_mov_b32_e32 v88, v10
	v_mov_b32_e32 v89, v10
	v_mov_b32_e32 v94, v10
	v_mov_b32_e32 v95, v10
	v_mov_b32_e32 v96, v10
	v_mov_b32_e32 v97, v10
	v_mov_b32_e32 v102, v10
	v_mov_b32_e32 v103, v10
	v_mov_b32_e32 v104, v10
	v_mov_b32_e32 v105, v10
	v_mov_b32_e32 v110, v10
	v_mov_b32_e32 v111, v10
	v_mov_b32_e32 v112, v10
	v_mov_b32_e32 v113, v10
	v_mov_b32_e32 v118, v10
	v_mov_b32_e32 v119, v10
	v_mov_b32_e32 v120, v10
	v_mov_b32_e32 v121, v10
	v_mov_b32_e32 v122, v10
	v_mov_b32_e32 v123, v10
	v_mov_b32_e32 v124, v10
	v_mov_b32_e32 v125, v10
	v_mov_b32_e32 v126, v10
	v_mov_b32_e32 v127, v10
	v_mov_b32_e32 v128, v10
	v_mov_b32_e32 v129, v10
	v_mov_b32_e32 v54, v10
	v_mov_b32_e32 v55, v10
	v_mov_b32_e32 v56, v10
	v_mov_b32_e32 v57, v10
	v_mov_b32_e32 v50, v10
	v_mov_b32_e32 v51, v10
	v_mov_b32_e32 v52, v10
	v_mov_b32_e32 v53, v10
	v_mov_b32_e32 v34, v10
	v_mov_b32_e32 v35, v10
	v_mov_b32_e32 v36, v10
	v_mov_b32_e32 v37, v10
	v_mov_b32_e32 v26, v10
	v_mov_b32_e32 v27, v10
	v_mov_b32_e32 v28, v10
	v_mov_b32_e32 v29, v10
	.p2align 6
	s_nop 0
	s_nop 0
	s_nop 0
	s_nop 0
	s_nop 0
	s_nop 0

.LBB0_1410:
	s_ashr_i32 s2, s71, 8
	s_lshl_b32 s1, s71, 8
	s_lshl_b32 s0, s2, 12
	s_and_b32 s1, s1, 0xf00
	s_bfe_u32 s72, s71, 0x40004
	s_or_b32 s34, s0, s1
	s_lshl_b32 s66, s72, 9
	s_ashr_i32 s35, s34, 31
	s_mul_i32 s1, s34, 0x1800
	s_mul_hi_i32 s0, s34, 0x1800
	s_add_u32 s1, s25, s1
	s_addc_u32 s3, s38, s0
	s_mul_i32 s0, s72, 0x180
	s_waitcnt vmcnt(0)
	v_mov_b32_e32 v12, v0
	s_add_u32 s0, s1, s0
	s_addc_u32 s1, s3, 0
	v_ashrrev_i32_e32 v13, 6, v12
	v_and_b32_e32 v155, 31, v12
	v_lshlrev_b32_e32 v158, 5, v13
	s_waitcnt lgkmcnt(0)
	v_bfe_u32 v176, v12, 5, 1
	v_or_b32_e32 v4, v158, v155
	v_mov_b64_e32 v[2:3], s[0:1]
	v_mad_i64_i32 v[2:3], s[0:1], v4, s45, v[2:3]
	v_lshlrev_b32_e32 v156, 4, v176
	v_lshl_add_u64 v[10:11], v[2:3], 0, v[156:157]
	global_load_dwordx4 v[2:5], v[10:11], off offset:320
	global_load_dwordx4 v[6:9], v[10:11], off offset:352
	global_load_dwordx4 v[134:137], v[10:11], off
	global_load_dwordx4 v[130:133], v[10:11], off offset:32
	global_load_dwordx4 v[126:129], v[10:11], off offset:64
	global_load_dwordx4 v[122:125], v[10:11], off offset:96
	global_load_dwordx4 v[118:121], v[10:11], off offset:128
	global_load_dwordx4 v[114:117], v[10:11], off offset:160
	global_load_dwordx4 v[110:113], v[10:11], off offset:192
	global_load_dwordx4 v[106:109], v[10:11], off offset:224
	global_load_dwordx4 v[102:105], v[10:11], off offset:256
	global_load_dwordx4 v[98:101], v[10:11], off offset:288
	s_mulk_i32 s2, 0x1100
	s_ashr_i32 s3, s2, 31
	s_lshl_b64 s[0:1], s[2:3], 13
	s_add_u32 s4, s39, s0
	s_addc_u32 s5, s40, s1
	s_add_u32 s36, s4, s66
	s_addc_u32 s37, s5, 0
	s_lshl_b64 s[4:5], s[2:3], 7
	v_lshlrev_b32_e32 v59, 3, v12
	v_readfirstlane_b32 s67, v13
	s_add_u32 s2, s41, s4
	v_and_b32_e32 v52, 63, v12
	v_mul_lo_u32 v16, v13, s45
	v_and_b32_e32 v13, 24, v59
	s_addc_u32 s3, s42, s5
	s_lshl_b32 s33, s67, 3
	s_lshl_b32 s64, s67, 2
	v_lshlrev_b32_e32 v64, 4, v52
	v_add_u32_e32 v16, s47, v16
	v_and_or_b32 v56, v12, 32, v13
	v_lshl_or_b32 v13, s67, 6, v52
	s_and_b32 s73, s33, -16
	s_and_b32 s74, s64, 4
	v_bfe_u32 v15, v12, 4, 2
	v_lshrrev_b32_e32 v14, 1, v12
	v_add_u32_e32 v180, v16, v64
	v_lshlrev_b32_e32 v16, 3, v13
	v_lshrrev_b32_e32 v13, 4, v13
	s_cmp_lg_u32 0, -1
	v_and_b32_e32 v54, 8, v14
	v_lshlrev_b32_e32 v14, 12, v15
	v_xor_b32_e32 v13, v13, v12
	v_or3_b32 v11, v15, s33, 4
	s_cselect_b32 s75, 0, 0
	s_lshl_b32 s33, s67, 11
	v_and_b32_e32 v17, 15, v12
	v_bitop3_b32 v18, v15, v12, 15 bitop3:0x78
	v_lshl_or_b32 v55, s67, 15, v14
	v_lshlrev_b32_e32 v13, 3, v13
	s_cmp_lg_u32 s49, -1
	v_bfe_u32 v53, v12, 2, 2
	v_lshl_or_b32 v14, v18, 3, v55
	v_and_b32_e32 v57, 56, v13
	v_bitop3_b32 v13, v11, v17, 7 bitop3:0x6c
	s_cselect_b32 s64, s49, 0
	v_mov_b32_e32 v15, v157
	v_or3_b32 v10, v54, v53, s73
	v_lshlrev_b32_e32 v58, 3, v13
	s_add_i32 s76, s33, s64
	s_add_i32 s64, s33, s75
	s_lshl_b32 s65, s67, 10
	v_lshlrev_b64 v[50:51], 1, v[14:15]
	v_or_b32_e32 v10, s74, v10
	v_lshl_or_b32 v18, v11, 12, v58
	s_cmp_lg_u32 s50, -1
	s_mov_b32 m0, s76
	v_mov_b32_e32 v19, v157
	v_lshl_or_b32 v10, v10, 12, v56
	s_cselect_b32 s77, s50, 0
	v_mov_b32_e32 v11, v157
	v_and_or_b32 v16, v16, s48, v57
	s_add_i32 s77, s65, s77
	s_waitcnt vmcnt(11)
	ds_write_b128 v180, v[2:5]
	s_waitcnt vmcnt(10)
	ds_write_b128 v180, v[6:9] offset:1024
	v_lshl_add_u64 v[2:3], s[36:37], 0, v[50:51]
	global_load_lds_dwordx4 v[2:3], off
	v_lshlrev_b64 v[2:3], 1, v[18:19]
	v_lshl_add_u64 v[4:5], s[36:37], 0, v[2:3]
	s_add_i32 m0, s76, 0x400
	v_mov_b32_e32 v17, v157
	v_lshlrev_b64 v[6:7], 1, v[10:11]
	global_load_lds_dwordx4 v[4:5], off
	v_lshl_add_u64 v[4:5], v[16:17], 1, s[2:3]
	s_mov_b32 m0, s77
	v_lshl_add_u64 v[8:9], s[36:37], 0, v[6:7]
	s_mov_b64 s[2:3], 0x100
	v_or_b32_e32 v20, 64, v10
	global_load_lds_dwordx4 v[4:5], off
	v_lshl_add_u64 v[10:11], v[8:9], 0, s[2:3]
	s_mov_b32 m0, s64
	s_mov_b64 s[2:3], 0x180
	global_load_lds_dwordx4 v[10:11], off
	s_add_i32 m0, s64, 0x400
	v_lshl_add_u64 v[8:9], v[8:9], 0, s[2:3]
	s_add_u32 s2, s36, 0x80000
	s_addc_u32 s3, s37, 0
	global_load_lds_dwordx4 v[8:9], off
	v_lshl_add_u64 v[8:9], s[2:3], 0, v[50:51]
	s_add_i32 m0, s76, 0x4000
	v_lshl_add_u64 v[2:3], s[2:3], 0, v[2:3]
	global_load_lds_dwordx4 v[8:9], off
	s_add_i32 m0, s76, 0x4400
	s_mov_b64 s[2:3], 0x2000
	global_load_lds_dwordx4 v[2:3], off
	s_add_i32 m0, s77, 0x2000
	v_lshl_add_u64 v[2:3], v[4:5], 0, s[2:3]
	s_add_u32 s2, s36, 0x80100
	s_addc_u32 s3, s37, 0
	v_mov_b32_e32 v21, v157
	global_load_lds_dwordx4 v[2:3], off
	v_lshl_add_u64 v[2:3], s[2:3], 0, v[6:7]
	s_add_i32 m0, s64, 0x4000
	v_lshlrev_b32_e32 v10, 8, v155
	global_load_lds_dwordx4 v[2:3], off
	v_lshl_add_u64 v[2:3], v[20:21], 1, s[2:3]
	s_add_i32 m0, s64, 0x4400
	v_or_b32_e32 v13, 32, v156
	global_load_lds_dwordx4 v[2:3], off
	v_lshlrev_b32_e32 v2, 4, v12
	v_and_b32_e32 v11, 0x70, v2
	v_bitop3_b32 v182, v156, v10, v11 bitop3:0xde
	v_add_u32_e32 v183, 0, v182
	s_waitcnt vmcnt(0)
	s_waitcnt vmcnt(0) lgkmcnt(0)
	s_barrier
	ds_read_b128 v[2:5], v183 offset:49152
	ds_read_b128 v[6:9], v183 offset:57344
	s_waitcnt lgkmcnt(1)
	v_mfma_f32_32x32x16_bf16 v[34:49], v[2:5], v[134:137], 0
	v_bitop3_b32 v184, v13, v10, v11 bitop3:0xde
	v_add_u32_e32 v185, 0, v184
	v_or_b32_e32 v14, 64, v156
	v_bitop3_b32 v186, v14, v10, v11 bitop3:0xde
	v_add_u32_e32 v187, 0, v186
	v_or_b32_e32 v65, 0x60, v156
	v_bitop3_b32 v188, v65, v10, v11 bitop3:0xde
	s_waitcnt lgkmcnt(0)
	v_mfma_f32_32x32x16_bf16 v[18:33], v[6:9], v[134:137], 0
	ds_read_b128 v[2:5], v185 offset:49152
	ds_read_b128 v[6:9], v185 offset:57344
	v_add_u32_e32 v189, 0, v188
	v_cmp_gt_u32_e64 s[2:3], 32, v52
	s_mov_b32 s36, -1
	s_mov_b32 s37, 0
	v_mov_b32_e32 v178, 0
	s_waitcnt lgkmcnt(1)
	v_mfma_f32_32x32x16_bf16 v[34:49], v[2:5], v[130:133], v[34:49]
	s_waitcnt lgkmcnt(0)
	v_mfma_f32_32x32x16_bf16 v[18:33], v[6:9], v[130:133], v[18:33]
	ds_read_b128 v[2:5], v187 offset:49152
	ds_read_b128 v[6:9], v187 offset:57344
	s_waitcnt lgkmcnt(1)
	v_mfma_f32_32x32x16_bf16 v[34:49], v[2:5], v[126:129], v[34:49]
	s_waitcnt lgkmcnt(0)
	v_mfma_f32_32x32x16_bf16 v[18:33], v[6:9], v[126:129], v[18:33]
	ds_read_b128 v[2:5], v189 offset:49152
	ds_read_b128 v[6:9], v189 offset:57344
	s_waitcnt lgkmcnt(1)
	v_mfma_f32_32x32x16_bf16 v[34:49], v[2:5], v[122:125], v[34:49]
	v_or_b32_e32 v2, 0x80, v156
	v_bitop3_b32 v190, v2, v10, v11 bitop3:0xde
	v_add_u32_e32 v191, 0, v190
	s_waitcnt lgkmcnt(0)
	v_mfma_f32_32x32x16_bf16 v[18:33], v[6:9], v[122:125], v[18:33]
	ds_read_b128 v[2:5], v191 offset:49152
	ds_read_b128 v[6:9], v191 offset:57344
	s_waitcnt lgkmcnt(1)
	v_mfma_f32_32x32x16_bf16 v[34:49], v[2:5], v[118:121], v[34:49]
	v_or_b32_e32 v2, 0xa0, v156
	v_bitop3_b32 v192, v2, v10, v11 bitop3:0xde
	v_add_u32_e32 v193, 0, v192
	s_waitcnt lgkmcnt(0)
	v_mfma_f32_32x32x16_bf16 v[18:33], v[6:9], v[118:121], v[18:33]
	ds_read_b128 v[2:5], v193 offset:49152
	ds_read_b128 v[6:9], v193 offset:57344
	s_waitcnt lgkmcnt(1)
	v_mfma_f32_32x32x16_bf16 v[34:49], v[2:5], v[114:117], v[34:49]
	v_or_b32_e32 v2, 0xc0, v156
	v_bitop3_b32 v194, v2, v10, v11 bitop3:0xde
	v_add_u32_e32 v195, 0, v194
	s_waitcnt lgkmcnt(0)
	v_mfma_f32_32x32x16_bf16 v[18:33], v[6:9], v[114:117], v[18:33]
	ds_read_b128 v[2:5], v195 offset:49152
	ds_read_b128 v[6:9], v195 offset:57344
	s_waitcnt lgkmcnt(1)
	v_mfma_f32_32x32x16_bf16 v[34:49], v[2:5], v[110:113], v[34:49]
	v_or_b32_e32 v2, 0xe0, v156
	v_bitop3_b32 v196, v2, v10, v11 bitop3:0xde
	v_add_u32_e32 v197, 0, v196
	v_lshlrev_b32_e32 v10, 7, v155
	v_and_b32_e32 v11, 0x70, v59
	v_bitop3_b32 v199, v156, v10, v11 bitop3:0xde
	v_add_u32_e32 v200, s50, v199
	s_waitcnt lgkmcnt(0)
	v_mfma_f32_32x32x16_bf16 v[18:33], v[6:9], v[110:113], v[18:33]
	ds_read_b128 v[2:5], v197 offset:49152
	ds_read_b128 v[6:9], v197 offset:57344
	v_bitop3_b32 v201, v13, v10, v11 bitop3:0xde
	v_add_u32_e32 v202, s50, v201
	v_bitop3_b32 v203, v14, v10, v11 bitop3:0xde
	v_add_u32_e32 v204, s50, v203
	v_bitop3_b32 v205, v65, v10, v11 bitop3:0xde
	v_add_u32_e32 v206, s50, v205
	s_waitcnt lgkmcnt(1)
	v_mfma_f32_32x32x16_bf16 v[34:49], v[2:5], v[106:109], v[34:49]
	v_lshlrev_b32_e32 v59, 3, v52
	s_waitcnt lgkmcnt(0)
	v_mfma_f32_32x32x16_bf16 v[18:33], v[6:9], v[106:109], v[18:33]
	ds_read_b128 v[2:5], v200
	ds_read_b128 v[6:9], v200 offset:4096
	s_waitcnt lgkmcnt(1)
	v_mfma_f32_32x32x16_bf16 v[34:49], v[2:5], v[102:105], v[34:49]
	s_waitcnt lgkmcnt(0)
	v_mfma_f32_32x32x16_bf16 v[18:33], v[6:9], v[102:105], v[18:33]
	ds_read_b128 v[2:5], v202
	ds_read_b128 v[6:9], v202 offset:4096
	s_waitcnt lgkmcnt(1)
	v_mfma_f32_32x32x16_bf16 v[34:49], v[2:5], v[98:101], v[34:49]
	s_waitcnt lgkmcnt(0)
	v_mfma_f32_32x32x16_bf16 v[18:33], v[6:9], v[98:101], v[18:33]
	ds_read_b128 v[2:5], v204
	ds_read_b128 v[6:9], v180
	ds_read_b128 v[14:17], v204 offset:4096
	ds_read_b128 v[60:63], v180 offset:1024
	s_waitcnt lgkmcnt(2)
	v_mfma_f32_32x32x16_bf16 v[34:49], v[2:5], v[6:9], v[34:49]
	ds_read_b128 v[2:5], v206
	s_waitcnt lgkmcnt(2)
	v_mfma_f32_32x32x16_bf16 v[18:33], v[14:17], v[6:9], v[18:33]
	v_and_b32_e32 v6, 0x3fffffc0, v12
	v_lshl_add_u32 v159, v6, 2, s46
	v_and_b32_e32 v6, 0xc0, v64
	ds_read_b128 v[64:67], v206 offset:4096
	v_lshl_add_u32 v177, v155, 2, v159
	s_waitcnt lgkmcnt(0)
	s_barrier
	v_mfma_f32_32x32x16_bf16 v[34:49], v[2:5], v[60:63], v[34:49]
	v_lshlrev_b32_e32 v3, 1, v12
	v_and_or_b32 v2, v59, 24, v6
	v_and_b32_e32 v3, 32, v3
	v_and_b32_e32 v4, 0x100, v59
	v_or3_b32 v179, v2, v3, v4
	v_mov_b64_e32 v[2:3], s[8:9]
	v_mov_b64_e32 v[16:17], s[22:23]
	v_mfma_f32_32x32x16_bf16 v[18:33], v[64:67], v[60:63], v[18:33]
	s_nop 3
	v_max_f32_e32 v60, v35, v35
	v_max_f32_e32 v61, v34, v34
	v_max_f32_e32 v60, v61, v60
	v_max3_f32 v60, v60, v36, v37
	v_max3_f32 v60, v60, v38, v39
	v_max3_f32 v60, v60, v40, v41
	v_max3_f32 v60, v60, v42, v43
	v_max3_f32 v60, v60, v44, v45
	v_max3_f32 v60, v60, v46, v47
	v_max3_f32 v60, v60, v48, v49
	v_max3_f32 v60, v60, v18, v19
	v_max3_f32 v60, v60, v20, v21
	v_max3_f32 v60, v60, v22, v23
	v_max3_f32 v60, v60, v24, v25
	v_max3_f32 v60, v60, v26, v27
	v_max3_f32 v60, v60, v28, v29
	v_max3_f32 v60, v60, v30, v31
	v_max3_f32 v60, v60, v32, v33
	v_mov_b32_e32 v61, v60
	s_nop 1
	v_permlane32_swap_b32_e32 v60, v61
	v_max_f32_e32 v61, v61, v61
	v_max_f32_e32 v60, v60, v60
	v_max_f32_e32 v60, v60, v61
	v_add_f32_e32 v61, 0x7149f2ca, v60
	v_max_f32_e32 v60, 0xf149f2ca, v60
	v_cmp_ge_f32_e32 vcc, s51, v61
	v_sub_f32_e32 v61, 0xf149f2ca, v60
	v_mul_f32_e32 v61, 0x3dd53b94, v61
	v_exp_f32_e32 v61, v61
	s_cmp_eq_u64 vcc, exec
	s_cselect_b64 vcc, -1, 0
	v_cndmask_b32_e32 v208, v60, v1, vcc
	v_mul_f32_e32 v60, 0xbdd53b94, v208
	v_cndmask_b32_e64 v207, v61, 1.0, vcc
	v_mov_b32_e32 v61, v60
	v_fmac_f32_e32 v61, 0x3dd53b94, v49
	v_pk_fma_f32 v[152:153], v[18:19], s[24:25], v[60:61] op_sel_hi:[1,0,0]
	v_lshl_or_b32 v18, s67, 9, v59
	v_and_or_b32 v18, v18, s48, v57
	v_mov_b32_e32 v19, v157
	v_lshl_add_u64 v[160:161], v[18:19], 1, s[4:5]
	v_or_b32_e32 v18, s73, v54
	v_fmamk_f32 v34, v34, 0x3dd53b94, v60
	v_fmamk_f32 v35, v35, 0x3dd53b94, v60
	v_fmamk_f32 v36, v36, 0x3dd53b94, v60
	v_fmamk_f32 v37, v37, 0x3dd53b94, v60
	v_fmamk_f32 v38, v38, 0x3dd53b94, v60
	v_fmamk_f32 v39, v39, 0x3dd53b94, v60
	v_fmamk_f32 v40, v40, 0x3dd53b94, v60
	v_fmamk_f32 v41, v41, 0x3dd53b94, v60
	v_fmamk_f32 v42, v42, 0x3dd53b94, v60
	v_fmamk_f32 v43, v43, 0x3dd53b94, v60
	v_fmamk_f32 v44, v44, 0x3dd53b94, v60
	v_fmamk_f32 v45, v45, 0x3dd53b94, v60
	v_fmamk_f32 v46, v46, 0x3dd53b94, v60
	v_fmamk_f32 v47, v47, 0x3dd53b94, v60
	v_fmamk_f32 v48, v48, 0x3dd53b94, v60
	v_or3_b32 v18, v18, s74, v53
	v_exp_f32_e32 v239, v34
	v_exp_f32_e32 v241, v35
	v_exp_f32_e32 v237, v36
	v_exp_f32_e32 v240, v37
	v_exp_f32_e32 v236, v38
	v_exp_f32_e32 v238, v39
	v_exp_f32_e32 v234, v40
	v_exp_f32_e32 v235, v41
	v_exp_f32_e32 v231, v42
	v_exp_f32_e32 v233, v43
	v_exp_f32_e32 v230, v44
	v_exp_f32_e32 v232, v45
	v_exp_f32_e32 v227, v46
	v_exp_f32_e32 v229, v47
	v_exp_f32_e32 v226, v48
	v_exp_f32_e32 v228, v61
	s_or_b32 s0, s0, s66
	v_lshl_or_b32 v18, v18, 12, v56
	s_movk_i32 s4, 0x4000
	v_lshl_add_u64 v[162:163], v[18:19], 1, s[0:1]
	v_or3_b32 v18, v55, v58, s4
	v_mov_b64_e32 v[4:5], s[10:11]
	v_mov_b64_e32 v[6:7], s[12:13]
	v_mov_b64_e32 v[8:9], s[14:15]
	v_mov_b64_e32 v[10:11], s[16:17]
	v_mov_b64_e32 v[12:13], s[18:19]
	v_mov_b64_e32 v[14:15], s[20:21]
	v_pk_fma_f32 v[138:139], v[32:33], s[24:25], v[60:61] op_sel_hi:[1,0,0]
	v_pk_fma_f32 v[140:141], v[30:31], s[24:25], v[60:61] op_sel_hi:[1,0,0]
	v_pk_fma_f32 v[142:143], v[28:29], s[24:25], v[60:61] op_sel_hi:[1,0,0]
	v_pk_fma_f32 v[144:145], v[26:27], s[24:25], v[60:61] op_sel_hi:[1,0,0]
	v_pk_fma_f32 v[146:147], v[24:25], s[24:25], v[60:61] op_sel_hi:[1,0,0]
	v_pk_fma_f32 v[148:149], v[22:23], s[24:25], v[60:61] op_sel_hi:[1,0,0]
	v_pk_fma_f32 v[150:151], v[20:21], s[24:25], v[60:61] op_sel_hi:[1,0,0]
	v_lshl_add_u64 v[164:165], s[0:1], 0, v[50:51]
	v_lshl_add_u64 v[166:167], v[18:19], 1, s[0:1]
	v_mov_b64_e32 v[64:65], v[16:17]
	v_mov_b64_e32 v[48:49], v[16:17]
	v_mov_b64_e32 v[32:33], v[16:17]
	v_add_u32_e32 v181, s75, v179
	v_mov_b64_e32 v[62:63], v[14:15]
	v_mov_b64_e32 v[60:61], v[12:13]
	v_mov_b64_e32 v[58:59], v[10:11]
	v_mov_b64_e32 v[56:57], v[8:9]
	v_mov_b64_e32 v[54:55], v[6:7]
	v_mov_b64_e32 v[52:53], v[4:5]
	v_mov_b64_e32 v[50:51], v[2:3]
	v_mov_b64_e32 v[46:47], v[14:15]
	v_mov_b64_e32 v[44:45], v[12:13]
	v_mov_b64_e32 v[42:43], v[10:11]
	v_mov_b64_e32 v[40:41], v[8:9]
	v_mov_b64_e32 v[38:39], v[6:7]
	v_mov_b64_e32 v[36:37], v[4:5]
	v_mov_b64_e32 v[34:35], v[2:3]
	v_mov_b64_e32 v[30:31], v[14:15]
	v_mov_b64_e32 v[28:29], v[12:13]
	v_mov_b64_e32 v[26:27], v[10:11]
	v_mov_b64_e32 v[24:25], v[8:9]
	v_mov_b64_e32 v[22:23], v[6:7]
	v_mov_b64_e32 v[20:21], v[4:5]
	v_mov_b64_e32 v[18:19], v[2:3]
	s_mov_b32 s66, 2
	.p2align 6
	s_nop 0
	s_nop 0
	s_nop 0
	s_nop 0
	s_nop 0
	s_nop 0

.LBB0_1496:
	v_mov_b32_e32 v143, v135
	v_mov_b32_e32 v145, v135
	s_add_u32 s27, s28, 0x10000
	v_mov_b32_e32 v10, 0
	s_addc_u32 s56, s29, 0
	v_lshl_add_u64 v[146:147], s[12:13], 0, v[142:143]
	v_lshl_add_u64 v[148:149], s[12:13], 0, v[144:145]
	s_mov_b32 s57, -2
	s_mov_b64 s[28:29], 0
	v_mov_b32_e32 v11, v10
	v_mov_b32_e32 v12, v10
	v_mov_b32_e32 v13, v10
	v_mov_b32_e32 v18, v10
	v_mov_b32_e32 v19, v10
	v_mov_b32_e32 v20, v10
	v_mov_b32_e32 v21, v10
	v_mov_b32_e32 v30, v10
	v_mov_b32_e32 v31, v10
	v_mov_b32_e32 v32, v10
	v_mov_b32_e32 v33, v10
	v_mov_b32_e32 v42, v10
	v_mov_b32_e32 v43, v10
	v_mov_b32_e32 v44, v10
	v_mov_b32_e32 v45, v10
	v_mov_b32_e32 v2, v10
	v_mov_b32_e32 v3, v10
	v_mov_b32_e32 v4, v10
	v_mov_b32_e32 v5, v10
	v_mov_b32_e32 v6, v10
	v_mov_b32_e32 v7, v10
	v_mov_b32_e32 v8, v10
	v_mov_b32_e32 v9, v10
	v_mov_b32_e32 v14, v10
	v_mov_b32_e32 v15, v10
	v_mov_b32_e32 v16, v10
	v_mov_b32_e32 v17, v10
	v_mov_b32_e32 v22, v10
	v_mov_b32_e32 v23, v10
	v_mov_b32_e32 v24, v10
	v_mov_b32_e32 v25, v10
	v_mov_b32_e32 v38, v10
	v_mov_b32_e32 v39, v10
	v_mov_b32_e32 v40, v10
	v_mov_b32_e32 v41, v10
	v_mov_b32_e32 v46, v10
	v_mov_b32_e32 v47, v10
	v_mov_b32_e32 v48, v10
	v_mov_b32_e32 v49, v10
	v_mov_b32_e32 v58, v10
	v_mov_b32_e32 v59, v10
	v_mov_b32_e32 v60, v10
	v_mov_b32_e32 v61, v10
	v_mov_b32_e32 v62, v10
	v_mov_b32_e32 v63, v10
	v_mov_b32_e32 v64, v10
	v_mov_b32_e32 v65, v10
	v_mov_b32_e32 v66, v10
	v_mov_b32_e32 v67, v10
	v_mov_b32_e32 v68, v10
	v_mov_b32_e32 v69, v10
	v_mov_b32_e32 v70, v10
	v_mov_b32_e32 v71, v10
	v_mov_b32_e32 v72, v10
	v_mov_b32_e32 v73, v10
	v_mov_b32_e32 v74, v10
	v_mov_b32_e32 v75, v10
	v_mov_b32_e32 v76, v10
	v_mov_b32_e32 v77, v10
	v_mov_b32_e32 v82, v10
	v_mov_b32_e32 v83, v10
	v_mov_b32_e32 v84, v10
	v_mov_b32_e32 v85, v10
	v_mov_b32_e32 v90, v10
	v_mov_b32_e32 v91, v10
	v_mov_b32_e32 v92, v10
	v_mov_b32_e32 v93, v10
	v_mov_b32_e32 v98, v10
	v_mov_b32_e32 v99, v10
	v_mov_b32_e32 v100, v10
	v_mov_b32_e32 v101, v10
	v_mov_b32_e32 v106, v10
	v_mov_b32_e32 v107, v10
	v_mov_b32_e32 v108, v10
	v_mov_b32_e32 v109, v10
	v_mov_b32_e32 v114, v10
	v_mov_b32_e32 v115, v10
	v_mov_b32_e32 v116, v10
	v_mov_b32_e32 v117, v10
	v_mov_b32_e32 v78, v10
	v_mov_b32_e32 v79, v10
	v_mov_b32_e32 v80, v10
	v_mov_b32_e32 v81, v10
	v_mov_b32_e32 v86, v10
	v_mov_b32_e32 v87, v10
	v_mov_b32_e32 v88, v10
	v_mov_b32_e32 v89, v10
	v_mov_b32_e32 v94, v10
	v_mov_b32_e32 v95, v10
	v_mov_b32_e32 v96, v10
	v_mov_b32_e32 v97, v10
	v_mov_b32_e32 v102, v10
	v_mov_b32_e32 v103, v10
	v_mov_b32_e32 v104, v10
	v_mov_b32_e32 v105, v10
	v_mov_b32_e32 v110, v10
	v_mov_b32_e32 v111, v10
	v_mov_b32_e32 v112, v10
	v_mov_b32_e32 v113, v10
	v_mov_b32_e32 v118, v10
	v_mov_b32_e32 v119, v10
	v_mov_b32_e32 v120, v10
	v_mov_b32_e32 v121, v10
	v_mov_b32_e32 v122, v10
	v_mov_b32_e32 v123, v10
	v_mov_b32_e32 v124, v10
	v_mov_b32_e32 v125, v10
	v_mov_b32_e32 v126, v10
	v_mov_b32_e32 v127, v10
	v_mov_b32_e32 v128, v10
	v_mov_b32_e32 v129, v10
	v_mov_b32_e32 v54, v10
	v_mov_b32_e32 v55, v10
	v_mov_b32_e32 v56, v10
	v_mov_b32_e32 v57, v10
	v_mov_b32_e32 v50, v10
	v_mov_b32_e32 v51, v10
	v_mov_b32_e32 v52, v10
	v_mov_b32_e32 v53, v10
	v_mov_b32_e32 v34, v10
	v_mov_b32_e32 v35, v10
	v_mov_b32_e32 v36, v10
	v_mov_b32_e32 v37, v10
	v_mov_b32_e32 v26, v10
	v_mov_b32_e32 v27, v10
	v_mov_b32_e32 v28, v10
	v_mov_b32_e32 v29, v10
	.p2align 6
	s_nop 0
	s_nop 0
	s_nop 0
	s_nop 0
	s_nop 0
	s_nop 0

.LBB0_1867:
	v_mov_b32_e32 v147, v139
	v_mov_b32_e32 v145, v139
	s_add_u32 s21, s0, 0x10000
	v_mov_b32_e32 v26, 0
	s_addc_u32 s23, s1, 0
	v_lshl_add_u64 v[150:151], s[14:15], 0, v[144:145]
	v_lshl_add_u64 v[152:153], s[14:15], 0, v[146:147]
	s_mov_b32 s51, -2
	s_mov_b64 s[0:1], 0
	v_mov_b32_e32 v27, v26
	v_mov_b32_e32 v28, v26
	v_mov_b32_e32 v29, v26
	v_mov_b32_e32 v34, v26
	v_mov_b32_e32 v35, v26
	v_mov_b32_e32 v36, v26
	v_mov_b32_e32 v37, v26
	v_mov_b32_e32 v50, v26
	v_mov_b32_e32 v51, v26
	v_mov_b32_e32 v52, v26
	v_mov_b32_e32 v53, v26
	v_mov_b32_e32 v58, v26
	v_mov_b32_e32 v59, v26
	v_mov_b32_e32 v60, v26
	v_mov_b32_e32 v61, v26
	v_mov_b32_e32 v2, v26
	v_mov_b32_e32 v3, v26
	v_mov_b32_e32 v4, v26
	v_mov_b32_e32 v5, v26
	v_mov_b32_e32 v6, v26
	v_mov_b32_e32 v7, v26
	v_mov_b32_e32 v8, v26
	v_mov_b32_e32 v9, v26
	v_mov_b32_e32 v10, v26
	v_mov_b32_e32 v11, v26
	v_mov_b32_e32 v12, v26
	v_mov_b32_e32 v13, v26
	v_mov_b32_e32 v18, v26
	v_mov_b32_e32 v19, v26
	v_mov_b32_e32 v20, v26
	v_mov_b32_e32 v21, v26
	v_mov_b32_e32 v30, v26
	v_mov_b32_e32 v31, v26
	v_mov_b32_e32 v32, v26
	v_mov_b32_e32 v33, v26
	v_mov_b32_e32 v46, v26
	v_mov_b32_e32 v47, v26
	v_mov_b32_e32 v48, v26
	v_mov_b32_e32 v49, v26
	v_mov_b32_e32 v54, v26
	v_mov_b32_e32 v55, v26
	v_mov_b32_e32 v56, v26
	v_mov_b32_e32 v57, v26
	v_mov_b32_e32 v62, v26
	v_mov_b32_e32 v63, v26
	v_mov_b32_e32 v64, v26
	v_mov_b32_e32 v65, v26
	v_mov_b32_e32 v66, v26
	v_mov_b32_e32 v67, v26
	v_mov_b32_e32 v68, v26
	v_mov_b32_e32 v69, v26
	v_mov_b32_e32 v74, v26
	v_mov_b32_e32 v75, v26
	v_mov_b32_e32 v76, v26
	v_mov_b32_e32 v77, v26
	v_mov_b32_e32 v82, v26
	v_mov_b32_e32 v83, v26
	v_mov_b32_e32 v84, v26
	v_mov_b32_e32 v85, v26
	v_mov_b32_e32 v90, v26
	v_mov_b32_e32 v91, v26
	v_mov_b32_e32 v92, v26
	v_mov_b32_e32 v93, v26
	v_mov_b32_e32 v98, v26
	v_mov_b32_e32 v99, v26
	v_mov_b32_e32 v100, v26
	v_mov_b32_e32 v101, v26
	v_mov_b32_e32 v106, v26
	v_mov_b32_e32 v107, v26
	v_mov_b32_e32 v108, v26
	v_mov_b32_e32 v109, v26
	v_mov_b32_e32 v114, v26
	v_mov_b32_e32 v115, v26
	v_mov_b32_e32 v116, v26
	v_mov_b32_e32 v117, v26
	v_mov_b32_e32 v122, v26
	v_mov_b32_e32 v123, v26
	v_mov_b32_e32 v124, v26
	v_mov_b32_e32 v125, v26
	v_mov_b32_e32 v70, v26
	v_mov_b32_e32 v71, v26
	v_mov_b32_e32 v72, v26
	v_mov_b32_e32 v73, v26
	v_mov_b32_e32 v78, v26
	v_mov_b32_e32 v79, v26
	v_mov_b32_e32 v80, v26
	v_mov_b32_e32 v81, v26
	v_mov_b32_e32 v86, v26
	v_mov_b32_e32 v87, v26
	v_mov_b32_e32 v88, v26
	v_mov_b32_e32 v89, v26
	v_mov_b32_e32 v94, v26
	v_mov_b32_e32 v95, v26
	v_mov_b32_e32 v96, v26
	v_mov_b32_e32 v97, v26
	v_mov_b32_e32 v102, v26
	v_mov_b32_e32 v103, v26
	v_mov_b32_e32 v104, v26
	v_mov_b32_e32 v105, v26
	v_mov_b32_e32 v110, v26
	v_mov_b32_e32 v111, v26
	v_mov_b32_e32 v112, v26
	v_mov_b32_e32 v113, v26
	v_mov_b32_e32 v118, v26
	v_mov_b32_e32 v119, v26
	v_mov_b32_e32 v120, v26
	v_mov_b32_e32 v121, v26
	v_mov_b32_e32 v126, v26
	v_mov_b32_e32 v127, v26
	v_mov_b32_e32 v128, v26
	v_mov_b32_e32 v129, v26
	v_mov_b32_e32 v42, v26
	v_mov_b32_e32 v43, v26
	v_mov_b32_e32 v44, v26
	v_mov_b32_e32 v45, v26
	v_mov_b32_e32 v38, v26
	v_mov_b32_e32 v39, v26
	v_mov_b32_e32 v40, v26
	v_mov_b32_e32 v41, v26
	v_mov_b32_e32 v22, v26
	v_mov_b32_e32 v23, v26
	v_mov_b32_e32 v24, v26
	v_mov_b32_e32 v25, v26
	v_mov_b32_e32 v14, v26
	v_mov_b32_e32 v15, v26
	v_mov_b32_e32 v16, v26
	v_mov_b32_e32 v17, v26
	.p2align 6
	s_nop 0
	s_nop 0
	s_nop 0
	s_nop 0
	s_nop 0
	s_nop 0

.LBB0_1944:
	v_mov_b32_e32 v145, v135
	v_mov_b32_e32 v143, v135
	s_add_u32 s27, s30, 0x10000
	v_mov_b32_e32 v10, 0
	s_addc_u32 s29, s31, 0
	v_lshl_add_u64 v[146:147], s[12:13], 0, v[142:143]
	v_lshl_add_u64 v[148:149], s[12:13], 0, v[144:145]
	s_mov_b32 s58, -2
	s_mov_b64 s[30:31], 0
	v_mov_b32_e32 v11, v10
	v_mov_b32_e32 v12, v10
	v_mov_b32_e32 v13, v10
	v_mov_b32_e32 v18, v10
	v_mov_b32_e32 v19, v10
	v_mov_b32_e32 v20, v10
	v_mov_b32_e32 v21, v10
	v_mov_b32_e32 v30, v10
	v_mov_b32_e32 v31, v10
	v_mov_b32_e32 v32, v10
	v_mov_b32_e32 v33, v10
	v_mov_b32_e32 v42, v10
	v_mov_b32_e32 v43, v10
	v_mov_b32_e32 v44, v10
	v_mov_b32_e32 v45, v10
	v_mov_b32_e32 v2, v10
	v_mov_b32_e32 v3, v10
	v_mov_b32_e32 v4, v10
	v_mov_b32_e32 v5, v10
	v_mov_b32_e32 v6, v10
	v_mov_b32_e32 v7, v10
	v_mov_b32_e32 v8, v10
	v_mov_b32_e32 v9, v10
	v_mov_b32_e32 v14, v10
	v_mov_b32_e32 v15, v10
	v_mov_b32_e32 v16, v10
	v_mov_b32_e32 v17, v10
	v_mov_b32_e32 v22, v10
	v_mov_b32_e32 v23, v10
	v_mov_b32_e32 v24, v10
	v_mov_b32_e32 v25, v10
	v_mov_b32_e32 v38, v10
	v_mov_b32_e32 v39, v10
	v_mov_b32_e32 v40, v10
	v_mov_b32_e32 v41, v10
	v_mov_b32_e32 v46, v10
	v_mov_b32_e32 v47, v10
	v_mov_b32_e32 v48, v10
	v_mov_b32_e32 v49, v10
	v_mov_b32_e32 v58, v10
	v_mov_b32_e32 v59, v10
	v_mov_b32_e32 v60, v10
	v_mov_b32_e32 v61, v10
	v_mov_b32_e32 v62, v10
	v_mov_b32_e32 v63, v10
	v_mov_b32_e32 v64, v10
	v_mov_b32_e32 v65, v10
	v_mov_b32_e32 v66, v10
	v_mov_b32_e32 v67, v10
	v_mov_b32_e32 v68, v10
	v_mov_b32_e32 v69, v10
	v_mov_b32_e32 v70, v10
	v_mov_b32_e32 v71, v10
	v_mov_b32_e32 v72, v10
	v_mov_b32_e32 v73, v10
	v_mov_b32_e32 v74, v10
	v_mov_b32_e32 v75, v10
	v_mov_b32_e32 v76, v10
	v_mov_b32_e32 v77, v10
	v_mov_b32_e32 v82, v10
	v_mov_b32_e32 v83, v10
	v_mov_b32_e32 v84, v10
	v_mov_b32_e32 v85, v10
	v_mov_b32_e32 v90, v10
	v_mov_b32_e32 v91, v10
	v_mov_b32_e32 v92, v10
	v_mov_b32_e32 v93, v10
	v_mov_b32_e32 v98, v10
	v_mov_b32_e32 v99, v10
	v_mov_b32_e32 v100, v10
	v_mov_b32_e32 v101, v10
	v_mov_b32_e32 v106, v10
	v_mov_b32_e32 v107, v10
	v_mov_b32_e32 v108, v10
	v_mov_b32_e32 v109, v10
	v_mov_b32_e32 v114, v10
	v_mov_b32_e32 v115, v10
	v_mov_b32_e32 v116, v10
	v_mov_b32_e32 v117, v10
	v_mov_b32_e32 v78, v10
	v_mov_b32_e32 v79, v10
	v_mov_b32_e32 v80, v10
	v_mov_b32_e32 v81, v10
	v_mov_b32_e32 v86, v10
	v_mov_b32_e32 v87, v10
	v_mov_b32_e32 v88, v10
	v_mov_b32_e32 v89, v10
	v_mov_b32_e32 v94, v10
	v_mov_b32_e32 v95, v10
	v_mov_b32_e32 v96, v10
	v_mov_b32_e32 v97, v10
	v_mov_b32_e32 v102, v10
	v_mov_b32_e32 v103, v10
	v_mov_b32_e32 v104, v10
	v_mov_b32_e32 v105, v10
	v_mov_b32_e32 v110, v10
	v_mov_b32_e32 v111, v10
	v_mov_b32_e32 v112, v10
	v_mov_b32_e32 v113, v10
	v_mov_b32_e32 v118, v10
	v_mov_b32_e32 v119, v10
	v_mov_b32_e32 v120, v10
	v_mov_b32_e32 v121, v10
	v_mov_b32_e32 v122, v10
	v_mov_b32_e32 v123, v10
	v_mov_b32_e32 v124, v10
	v_mov_b32_e32 v125, v10
	v_mov_b32_e32 v126, v10
	v_mov_b32_e32 v127, v10
	v_mov_b32_e32 v128, v10
	v_mov_b32_e32 v129, v10
	v_mov_b32_e32 v54, v10
	v_mov_b32_e32 v55, v10
	v_mov_b32_e32 v56, v10
	v_mov_b32_e32 v57, v10
	v_mov_b32_e32 v50, v10
	v_mov_b32_e32 v51, v10
	v_mov_b32_e32 v52, v10
	v_mov_b32_e32 v53, v10
	v_mov_b32_e32 v34, v10
	v_mov_b32_e32 v35, v10
	v_mov_b32_e32 v36, v10
	v_mov_b32_e32 v37, v10
	v_mov_b32_e32 v26, v10
	v_mov_b32_e32 v27, v10
	v_mov_b32_e32 v28, v10
	v_mov_b32_e32 v29, v10
	.p2align 6
	s_nop 0
	s_nop 0
	s_nop 0
	s_nop 0
	s_nop 0
	s_nop 0
